# all-in with roperf: rope cos/sin of the next row group prefetched one block ahead in the layer-1 QKV epilogue (plus the bj=1 reuse)
# speedup vs baseline: 1.0050x; 1.0050x over previous
.LBB0_973:
	s_and_b32 s98, s46, 3
	s_lshl_b32 s98, s98, 1
	s_mov_b32 s99, s47
	v_and_b32_e32 v250, 63, v0
	v_and_b32_e32 v251, 15, v250
	v_lshrrev_b32_e32 v249, 4, v250
	v_readfirstlane_b32 s100, v0
	s_lshr_b32 s100, s100, 6
	s_lshl_b32 s101, s100, 11
	s_add_i32 s101, s101, 0xc000
	v_lshl_add_u32 v245, v250, 4, s101
	v_lshrrev_b32_e32 v248, 2, v251
	v_xor_b32_e32 v248, v248, v249
	v_and_b32_e32 v248, 1, v248
	v_lshlrev_b32_e32 v248, 5, v248
	v_lshl_add_u32 v248, v249, 9, v248
	v_and_b32_e32 v247, 3, v251
	v_add_u32_e32 v248, v248, v247
	v_lshrrev_b32_e32 v247, 3, v251
	v_lshl_add_u32 v248, v247, 2, v248
	v_add_u32_e32 v244, s101, v248
	s_and_b32 s101, s100, 3
	s_lshl_b32 s101, s101, 11
	v_lshl_add_u32 v252, v250, 4, s101
	s_ashr_i32 s6, s46, 2
	s_cmp_gt_i32 s6, 1
	s_cselect_b64 s[42:43], -1, 0
	s_cmp_lt_i32 s6, 2
	v_lshl_add_u32 v6, s47, 8, v200
	s_cselect_b64 s[4:5], -1, 0
	s_cmpk_lt_i32 s47, 0x80
	v_lshrrev_b32_e32 v2, 1, v201
	s_cselect_b64 s[44:45], -1, 0
	v_and_b32_e32 v30, 28, v2
	v_lshlrev_b32_e32 v2, 5, v6
	v_and_or_b32 v2, v2, s64, v30
	s_and_b64 s[44:45], s[4:5], s[44:45]
	v_lshlrev_b32_e32 v194, 3, v2
	v_cndmask_b32_e64 v2, 0, 1, s[44:45]
	v_pk_mul_f32 v[24:25], v[192:193], s[28:29] op_sel_hi:[1,0]
	v_pk_mul_f32 v[18:19], v[190:191], s[28:29] op_sel_hi:[1,0]
	v_pk_mul_f32 v[22:23], v[188:189], s[28:29] op_sel_hi:[1,0]
	v_pk_mul_f32 v[20:21], v[186:187], s[28:29] op_sel_hi:[1,0]
	v_cmp_ne_u32_e64 s[4:5], 1, v2
	s_andn2_b64 vcc, exec, s[44:45]
	v_lshl_add_u64 v[14:15], s[18:19], 0, v[194:195]
	s_cbranch_vccnz .LBB0_975
	global_load_dwordx4 v[2:5], v[14:15], off
	global_load_dwordx4 v[8:11], v[14:15], off offset:16
	s_mov_b32 s100, 0x1000
	s_mov_b32 s101, 0
	v_lshl_add_u64 v[240:241], v[14:15], 0, s[100:101]
	global_load_dwordx4 v[232:235], v[240:241], off
	global_load_dwordx4 v[236:239], v[240:241], off offset:16
	s_waitcnt vmcnt(3)
	v_mov_b32_e32 v224, v2
	v_mov_b32_e32 v225, v3
	v_mov_b32_e32 v226, v4
	v_mov_b32_e32 v227, v5
	v_pk_mul_f32 v[16:17], v[18:19], v[2:3] op_sel:[1,1] op_sel_hi:[1,0]
	v_mul_f32_e32 v32, v25, v5
	v_mul_f32_e32 v34, v25, v4
	s_waitcnt vmcnt(2)
	v_mov_b32_e32 v228, v8
	v_mov_b32_e32 v229, v9
	v_mov_b32_e32 v230, v10
	v_mov_b32_e32 v231, v11
	v_pk_mul_f32 v[38:39], v[20:21], v[8:9] op_sel:[1,1] op_sel_hi:[1,0]
	v_mul_f32_e32 v40, v23, v11
	v_mul_f32_e32 v42, v23, v10
	v_pk_mul_f32 v[12:13], v[18:19], v[2:3]
	v_pk_mul_f32 v[36:37], v[20:21], v[8:9]
	v_pk_fma_f32 v[18:19], v[18:19], v[2:3], v[16:17] op_sel_hi:[0,1,1]
	v_pk_fma_f32 v[2:3], v[24:25], v[4:5], v[32:33] op_sel_hi:[1,1,0] neg_lo:[0,0,1] neg_hi:[0,0,1]
	v_pk_fma_f32 v[4:5], v[24:25], v[4:5], v[34:35] op_sel:[0,1,0] op_sel_hi:[1,0,0]
	v_pk_fma_f32 v[20:21], v[20:21], v[8:9], v[38:39] op_sel_hi:[0,1,1]
	v_pk_fma_f32 v[8:9], v[22:23], v[10:11], v[40:41] op_sel_hi:[1,1,0] neg_lo:[0,0,1] neg_hi:[0,0,1]
	v_pk_fma_f32 v[10:11], v[22:23], v[10:11], v[42:43] op_sel:[0,1,0] op_sel_hi:[1,0,0]
	v_sub_f32_e32 v20, v36, v38
	v_sub_f32_e32 v18, v12, v16
	v_mov_b32_e32 v22, v8
	v_mov_b32_e32 v23, v10
	v_mov_b32_e32 v24, v2
	v_mov_b32_e32 v25, v4

.LBB0_985:
	v_or_b32_e32 v14, 16, v6
	v_lshlrev_b32_e32 v7, 5, v14
	v_and_or_b32 v7, v7, s65, v30
	v_lshlrev_b32_e32 v194, 3, v7
	v_pk_mul_f32 v[24:25], v[176:177], s[28:29] op_sel_hi:[1,0]
	v_pk_mul_f32 v[18:19], v[174:175], s[28:29] op_sel_hi:[1,0]
	v_pk_mul_f32 v[22:23], v[172:173], s[28:29] op_sel_hi:[1,0]
	v_pk_mul_f32 v[20:21], v[170:171], s[28:29] op_sel_hi:[1,0]
	s_and_b64 vcc, exec, s[4:5]
	v_lshl_add_u64 v[16:17], s[18:19], 0, v[194:195]
	s_cbranch_vccnz .LBB0_987
	s_waitcnt vmcnt(2)
	v_mov_b32_e32 v32, v232
	v_mov_b32_e32 v33, v233
	v_mov_b32_e32 v34, v234
	v_mov_b32_e32 v35, v235
	v_mov_b32_e32 v36, v236
	v_mov_b32_e32 v37, v237
	v_mov_b32_e32 v38, v238
	v_mov_b32_e32 v39, v239
	s_mov_b32 s100, 0x1000
	s_mov_b32 s101, 0
	v_lshl_add_u64 v[240:241], v[16:17], 0, s[100:101]
	global_load_dwordx4 v[232:235], v[240:241], off
	global_load_dwordx4 v[236:239], v[240:241], off offset:16
	v_mov_b32_e32 v224, v32
	v_mov_b32_e32 v225, v33
	v_mov_b32_e32 v226, v34
	v_mov_b32_e32 v227, v35
	v_mov_b32_e32 v228, v36
	v_mov_b32_e32 v229, v37
	v_mov_b32_e32 v230, v38
	v_mov_b32_e32 v231, v39
	v_pk_mul_f32 v[40:41], v[18:19], v[32:33] op_sel:[1,1] op_sel_hi:[1,0]
	v_mul_f32_e32 v42, v25, v35
	v_mul_f32_e32 v44, v25, v34
	v_pk_mul_f32 v[48:49], v[20:21], v[36:37] op_sel:[1,1] op_sel_hi:[1,0]
	v_mul_f32_e32 v50, v23, v39
	v_mul_f32_e32 v52, v23, v38
	v_pk_mul_f32 v[12:13], v[18:19], v[32:33]
	v_pk_mul_f32 v[46:47], v[20:21], v[36:37]
	v_pk_fma_f32 v[18:19], v[18:19], v[32:33], v[40:41] op_sel_hi:[0,1,1]
	v_pk_fma_f32 v[32:33], v[24:25], v[34:35], v[42:43] op_sel_hi:[1,1,0] neg_lo:[0,0,1] neg_hi:[0,0,1]
	v_pk_fma_f32 v[34:35], v[24:25], v[34:35], v[44:45] op_sel:[0,1,0] op_sel_hi:[1,0,0]
	v_pk_fma_f32 v[20:21], v[20:21], v[36:37], v[48:49] op_sel_hi:[0,1,1]
	v_pk_fma_f32 v[24:25], v[22:23], v[38:39], v[50:51] op_sel_hi:[1,1,0] neg_lo:[0,0,1] neg_hi:[0,0,1]
	v_pk_fma_f32 v[36:37], v[22:23], v[38:39], v[52:53] op_sel:[0,1,0] op_sel_hi:[1,0,0]
	v_sub_f32_e32 v20, v46, v48
	v_sub_f32_e32 v18, v12, v40
	v_mov_b32_e32 v22, v24
	v_mov_b32_e32 v23, v36
	v_mov_b32_e32 v24, v32
	v_mov_b32_e32 v25, v34

.LBB0_995:
	v_or_b32_e32 v14, 32, v6
	v_lshlrev_b32_e32 v7, 5, v14
	v_and_or_b32 v7, v7, s66, v30
	v_lshlrev_b32_e32 v194, 3, v7
	v_pk_mul_f32 v[24:25], v[160:161], s[28:29] op_sel_hi:[1,0]
	v_pk_mul_f32 v[18:19], v[158:159], s[28:29] op_sel_hi:[1,0]
	v_pk_mul_f32 v[22:23], v[156:157], s[28:29] op_sel_hi:[1,0]
	v_pk_mul_f32 v[20:21], v[154:155], s[28:29] op_sel_hi:[1,0]
	s_and_b64 vcc, exec, s[4:5]
	v_lshl_add_u64 v[16:17], s[18:19], 0, v[194:195]
	s_cbranch_vccnz .LBB0_997
	s_waitcnt vmcnt(2)
	v_mov_b32_e32 v32, v232
	v_mov_b32_e32 v33, v233
	v_mov_b32_e32 v34, v234
	v_mov_b32_e32 v35, v235
	v_mov_b32_e32 v36, v236
	v_mov_b32_e32 v37, v237
	v_mov_b32_e32 v38, v238
	v_mov_b32_e32 v39, v239
	s_mov_b32 s100, 0x1000
	s_mov_b32 s101, 0
	v_lshl_add_u64 v[240:241], v[16:17], 0, s[100:101]
	global_load_dwordx4 v[232:235], v[240:241], off
	global_load_dwordx4 v[236:239], v[240:241], off offset:16
	v_mov_b32_e32 v224, v32
	v_mov_b32_e32 v225, v33
	v_mov_b32_e32 v226, v34
	v_mov_b32_e32 v227, v35
	v_mov_b32_e32 v228, v36
	v_mov_b32_e32 v229, v37
	v_mov_b32_e32 v230, v38
	v_mov_b32_e32 v231, v39
	v_pk_mul_f32 v[40:41], v[18:19], v[32:33] op_sel:[1,1] op_sel_hi:[1,0]
	v_mul_f32_e32 v42, v25, v35
	v_mul_f32_e32 v44, v25, v34
	v_pk_mul_f32 v[48:49], v[20:21], v[36:37] op_sel:[1,1] op_sel_hi:[1,0]
	v_mul_f32_e32 v50, v23, v39
	v_mul_f32_e32 v52, v23, v38
	v_pk_mul_f32 v[12:13], v[18:19], v[32:33]
	v_pk_mul_f32 v[46:47], v[20:21], v[36:37]
	v_pk_fma_f32 v[18:19], v[18:19], v[32:33], v[40:41] op_sel_hi:[0,1,1]
	v_pk_fma_f32 v[32:33], v[24:25], v[34:35], v[42:43] op_sel_hi:[1,1,0] neg_lo:[0,0,1] neg_hi:[0,0,1]
	v_pk_fma_f32 v[34:35], v[24:25], v[34:35], v[44:45] op_sel:[0,1,0] op_sel_hi:[1,0,0]
	v_pk_fma_f32 v[20:21], v[20:21], v[36:37], v[48:49] op_sel_hi:[0,1,1]
	v_pk_fma_f32 v[24:25], v[22:23], v[38:39], v[50:51] op_sel_hi:[1,1,0] neg_lo:[0,0,1] neg_hi:[0,0,1]
	v_pk_fma_f32 v[36:37], v[22:23], v[38:39], v[52:53] op_sel:[0,1,0] op_sel_hi:[1,0,0]
	v_sub_f32_e32 v20, v46, v48
	v_sub_f32_e32 v18, v12, v40
	v_mov_b32_e32 v22, v24
	v_mov_b32_e32 v23, v36
	v_mov_b32_e32 v24, v32
	v_mov_b32_e32 v25, v34

.LBB0_1005:
	v_or_b32_e32 v14, 48, v6
	v_lshlrev_b32_e32 v7, 5, v14
	v_and_or_b32 v7, v7, s67, v30
	v_lshlrev_b32_e32 v194, 3, v7
	v_pk_mul_f32 v[24:25], v[144:145], s[28:29] op_sel_hi:[1,0]
	v_pk_mul_f32 v[18:19], v[142:143], s[28:29] op_sel_hi:[1,0]
	v_pk_mul_f32 v[22:23], v[140:141], s[28:29] op_sel_hi:[1,0]
	v_pk_mul_f32 v[20:21], v[138:139], s[28:29] op_sel_hi:[1,0]
	s_and_b64 vcc, exec, s[4:5]
	v_lshl_add_u64 v[16:17], s[18:19], 0, v[194:195]
	s_cbranch_vccnz .LBB0_1007
	s_waitcnt vmcnt(2)
	v_mov_b32_e32 v32, v232
	v_mov_b32_e32 v33, v233
	v_mov_b32_e32 v34, v234
	v_mov_b32_e32 v35, v235
	v_mov_b32_e32 v36, v236
	v_mov_b32_e32 v37, v237
	v_mov_b32_e32 v38, v238
	v_mov_b32_e32 v39, v239
	s_mov_b32 s100, 0x5000
	s_mov_b32 s101, 0
	v_lshl_add_u64 v[240:241], v[16:17], 0, s[100:101]
	global_load_dwordx4 v[232:235], v[240:241], off
	global_load_dwordx4 v[236:239], v[240:241], off offset:16
	v_mov_b32_e32 v224, v32
	v_mov_b32_e32 v225, v33
	v_mov_b32_e32 v226, v34
	v_mov_b32_e32 v227, v35
	v_mov_b32_e32 v228, v36
	v_mov_b32_e32 v229, v37
	v_mov_b32_e32 v230, v38
	v_mov_b32_e32 v231, v39
	v_pk_mul_f32 v[40:41], v[18:19], v[32:33] op_sel:[1,1] op_sel_hi:[1,0]
	v_mul_f32_e32 v42, v25, v35
	v_mul_f32_e32 v44, v25, v34
	v_pk_mul_f32 v[48:49], v[20:21], v[36:37] op_sel:[1,1] op_sel_hi:[1,0]
	v_mul_f32_e32 v50, v23, v39
	v_mul_f32_e32 v52, v23, v38
	v_pk_mul_f32 v[12:13], v[18:19], v[32:33]
	v_pk_mul_f32 v[46:47], v[20:21], v[36:37]
	v_pk_fma_f32 v[18:19], v[18:19], v[32:33], v[40:41] op_sel_hi:[0,1,1]
	v_pk_fma_f32 v[32:33], v[24:25], v[34:35], v[42:43] op_sel_hi:[1,1,0] neg_lo:[0,0,1] neg_hi:[0,0,1]
	v_pk_fma_f32 v[34:35], v[24:25], v[34:35], v[44:45] op_sel:[0,1,0] op_sel_hi:[1,0,0]
	v_pk_fma_f32 v[20:21], v[20:21], v[36:37], v[48:49] op_sel_hi:[0,1,1]
	v_pk_fma_f32 v[24:25], v[22:23], v[38:39], v[50:51] op_sel_hi:[1,1,0] neg_lo:[0,0,1] neg_hi:[0,0,1]
	v_pk_fma_f32 v[36:37], v[22:23], v[38:39], v[52:53] op_sel:[0,1,0] op_sel_hi:[1,0,0]
	v_sub_f32_e32 v20, v46, v48
	v_sub_f32_e32 v18, v12, v40
	v_mov_b32_e32 v22, v24
	v_mov_b32_e32 v23, v36
	v_mov_b32_e32 v24, v32
	v_mov_b32_e32 v25, v34

.LBB0_1015:
	v_add_u32_e32 v14, 0x80, v6
	v_lshlrev_b32_e32 v7, 5, v14
	v_and_or_b32 v7, v7, s64, v30
	v_lshlrev_b32_e32 v194, 3, v7
	v_pk_mul_f32 v[24:25], v[128:129], s[28:29] op_sel_hi:[1,0]
	v_pk_mul_f32 v[18:19], v[126:127], s[28:29] op_sel_hi:[1,0]
	v_pk_mul_f32 v[22:23], v[124:125], s[28:29] op_sel_hi:[1,0]
	v_pk_mul_f32 v[20:21], v[122:123], s[28:29] op_sel_hi:[1,0]
	s_and_b64 vcc, exec, s[4:5]
	v_lshl_add_u64 v[16:17], s[18:19], 0, v[194:195]
	s_cbranch_vccnz .LBB0_1017
	s_waitcnt vmcnt(2)
	v_mov_b32_e32 v32, v232
	v_mov_b32_e32 v33, v233
	v_mov_b32_e32 v34, v234
	v_mov_b32_e32 v35, v235
	v_mov_b32_e32 v36, v236
	v_mov_b32_e32 v37, v237
	v_mov_b32_e32 v38, v238
	v_mov_b32_e32 v39, v239
	s_mov_b32 s100, 0x1000
	s_mov_b32 s101, 0
	v_lshl_add_u64 v[240:241], v[16:17], 0, s[100:101]
	global_load_dwordx4 v[232:235], v[240:241], off
	global_load_dwordx4 v[236:239], v[240:241], off offset:16
	v_mov_b32_e32 v224, v32
	v_mov_b32_e32 v225, v33
	v_mov_b32_e32 v226, v34
	v_mov_b32_e32 v227, v35
	v_mov_b32_e32 v228, v36
	v_mov_b32_e32 v229, v37
	v_mov_b32_e32 v230, v38
	v_mov_b32_e32 v231, v39
	v_pk_mul_f32 v[40:41], v[18:19], v[32:33] op_sel:[1,1] op_sel_hi:[1,0]
	v_mul_f32_e32 v42, v25, v35
	v_mul_f32_e32 v44, v25, v34
	v_pk_mul_f32 v[48:49], v[20:21], v[36:37] op_sel:[1,1] op_sel_hi:[1,0]
	v_mul_f32_e32 v50, v23, v39
	v_mul_f32_e32 v52, v23, v38
	v_pk_mul_f32 v[12:13], v[18:19], v[32:33]
	v_pk_mul_f32 v[46:47], v[20:21], v[36:37]
	v_pk_fma_f32 v[18:19], v[18:19], v[32:33], v[40:41] op_sel_hi:[0,1,1]
	v_pk_fma_f32 v[32:33], v[24:25], v[34:35], v[42:43] op_sel_hi:[1,1,0] neg_lo:[0,0,1] neg_hi:[0,0,1]
	v_pk_fma_f32 v[34:35], v[24:25], v[34:35], v[44:45] op_sel:[0,1,0] op_sel_hi:[1,0,0]
	v_pk_fma_f32 v[20:21], v[20:21], v[36:37], v[48:49] op_sel_hi:[0,1,1]
	v_pk_fma_f32 v[24:25], v[22:23], v[38:39], v[50:51] op_sel_hi:[1,1,0] neg_lo:[0,0,1] neg_hi:[0,0,1]
	v_pk_fma_f32 v[36:37], v[22:23], v[38:39], v[52:53] op_sel:[0,1,0] op_sel_hi:[1,0,0]
	v_sub_f32_e32 v20, v46, v48
	v_sub_f32_e32 v18, v12, v40
	v_mov_b32_e32 v22, v24
	v_mov_b32_e32 v23, v36
	v_mov_b32_e32 v24, v32
	v_mov_b32_e32 v25, v34

.LBB0_1025:
	v_add_u32_e32 v14, 0x90, v6
	v_lshlrev_b32_e32 v7, 5, v14
	v_and_or_b32 v7, v7, s65, v30
	v_lshlrev_b32_e32 v194, 3, v7
	v_pk_mul_f32 v[24:25], v[112:113], s[28:29] op_sel_hi:[1,0]
	v_pk_mul_f32 v[18:19], v[110:111], s[28:29] op_sel_hi:[1,0]
	v_pk_mul_f32 v[22:23], v[108:109], s[28:29] op_sel_hi:[1,0]
	v_pk_mul_f32 v[20:21], v[106:107], s[28:29] op_sel_hi:[1,0]
	s_and_b64 vcc, exec, s[4:5]
	v_lshl_add_u64 v[16:17], s[18:19], 0, v[194:195]
	s_cbranch_vccnz .LBB0_1027
	s_waitcnt vmcnt(2)
	v_mov_b32_e32 v32, v232
	v_mov_b32_e32 v33, v233
	v_mov_b32_e32 v34, v234
	v_mov_b32_e32 v35, v235
	v_mov_b32_e32 v36, v236
	v_mov_b32_e32 v37, v237
	v_mov_b32_e32 v38, v238
	v_mov_b32_e32 v39, v239
	s_mov_b32 s100, 0x1000
	s_mov_b32 s101, 0
	v_lshl_add_u64 v[240:241], v[16:17], 0, s[100:101]
	global_load_dwordx4 v[232:235], v[240:241], off
	global_load_dwordx4 v[236:239], v[240:241], off offset:16
	v_mov_b32_e32 v224, v32
	v_mov_b32_e32 v225, v33
	v_mov_b32_e32 v226, v34
	v_mov_b32_e32 v227, v35
	v_mov_b32_e32 v228, v36
	v_mov_b32_e32 v229, v37
	v_mov_b32_e32 v230, v38
	v_mov_b32_e32 v231, v39
	v_pk_mul_f32 v[40:41], v[18:19], v[32:33] op_sel:[1,1] op_sel_hi:[1,0]
	v_mul_f32_e32 v42, v25, v35
	v_mul_f32_e32 v44, v25, v34
	v_pk_mul_f32 v[48:49], v[20:21], v[36:37] op_sel:[1,1] op_sel_hi:[1,0]
	v_mul_f32_e32 v50, v23, v39
	v_mul_f32_e32 v52, v23, v38
	v_pk_mul_f32 v[12:13], v[18:19], v[32:33]
	v_pk_mul_f32 v[46:47], v[20:21], v[36:37]
	v_pk_fma_f32 v[18:19], v[18:19], v[32:33], v[40:41] op_sel_hi:[0,1,1]
	v_pk_fma_f32 v[32:33], v[24:25], v[34:35], v[42:43] op_sel_hi:[1,1,0] neg_lo:[0,0,1] neg_hi:[0,0,1]
	v_pk_fma_f32 v[34:35], v[24:25], v[34:35], v[44:45] op_sel:[0,1,0] op_sel_hi:[1,0,0]
	v_pk_fma_f32 v[20:21], v[20:21], v[36:37], v[48:49] op_sel_hi:[0,1,1]
	v_pk_fma_f32 v[24:25], v[22:23], v[38:39], v[50:51] op_sel_hi:[1,1,0] neg_lo:[0,0,1] neg_hi:[0,0,1]
	v_pk_fma_f32 v[36:37], v[22:23], v[38:39], v[52:53] op_sel:[0,1,0] op_sel_hi:[1,0,0]
	v_sub_f32_e32 v20, v46, v48
	v_sub_f32_e32 v18, v12, v40
	v_mov_b32_e32 v22, v24
	v_mov_b32_e32 v23, v36
	v_mov_b32_e32 v24, v32
	v_mov_b32_e32 v25, v34

.LBB0_1035:
	v_add_u32_e32 v14, 0xa0, v6
	v_lshlrev_b32_e32 v7, 5, v14
	v_and_or_b32 v7, v7, s66, v30
	v_lshlrev_b32_e32 v194, 3, v7
	v_pk_mul_f32 v[24:25], v[96:97], s[28:29] op_sel_hi:[1,0]
	v_pk_mul_f32 v[18:19], v[94:95], s[28:29] op_sel_hi:[1,0]
	v_pk_mul_f32 v[22:23], v[92:93], s[28:29] op_sel_hi:[1,0]
	v_pk_mul_f32 v[20:21], v[90:91], s[28:29] op_sel_hi:[1,0]
	s_and_b64 vcc, exec, s[4:5]
	v_lshl_add_u64 v[16:17], s[18:19], 0, v[194:195]
	s_cbranch_vccnz .LBB0_1037
	s_waitcnt vmcnt(2)
	v_mov_b32_e32 v32, v232
	v_mov_b32_e32 v33, v233
	v_mov_b32_e32 v34, v234
	v_mov_b32_e32 v35, v235
	v_mov_b32_e32 v36, v236
	v_mov_b32_e32 v37, v237
	v_mov_b32_e32 v38, v238
	v_mov_b32_e32 v39, v239
	s_mov_b32 s100, 0x1000
	s_mov_b32 s101, 0
	v_lshl_add_u64 v[240:241], v[16:17], 0, s[100:101]
	global_load_dwordx4 v[232:235], v[240:241], off
	global_load_dwordx4 v[236:239], v[240:241], off offset:16
	v_mov_b32_e32 v224, v32
	v_mov_b32_e32 v225, v33
	v_mov_b32_e32 v226, v34
	v_mov_b32_e32 v227, v35
	v_mov_b32_e32 v228, v36
	v_mov_b32_e32 v229, v37
	v_mov_b32_e32 v230, v38
	v_mov_b32_e32 v231, v39
	v_pk_mul_f32 v[40:41], v[18:19], v[32:33] op_sel:[1,1] op_sel_hi:[1,0]
	v_mul_f32_e32 v42, v25, v35
	v_mul_f32_e32 v44, v25, v34
	v_pk_mul_f32 v[48:49], v[20:21], v[36:37] op_sel:[1,1] op_sel_hi:[1,0]
	v_mul_f32_e32 v50, v23, v39
	v_mul_f32_e32 v52, v23, v38
	v_pk_mul_f32 v[12:13], v[18:19], v[32:33]
	v_pk_mul_f32 v[46:47], v[20:21], v[36:37]
	v_pk_fma_f32 v[18:19], v[18:19], v[32:33], v[40:41] op_sel_hi:[0,1,1]
	v_pk_fma_f32 v[32:33], v[24:25], v[34:35], v[42:43] op_sel_hi:[1,1,0] neg_lo:[0,0,1] neg_hi:[0,0,1]
	v_pk_fma_f32 v[34:35], v[24:25], v[34:35], v[44:45] op_sel:[0,1,0] op_sel_hi:[1,0,0]
	v_pk_fma_f32 v[20:21], v[20:21], v[36:37], v[48:49] op_sel_hi:[0,1,1]
	v_pk_fma_f32 v[24:25], v[22:23], v[38:39], v[50:51] op_sel_hi:[1,1,0] neg_lo:[0,0,1] neg_hi:[0,0,1]
	v_pk_fma_f32 v[36:37], v[22:23], v[38:39], v[52:53] op_sel:[0,1,0] op_sel_hi:[1,0,0]
	v_sub_f32_e32 v20, v46, v48
	v_sub_f32_e32 v18, v12, v40
	v_mov_b32_e32 v22, v24
	v_mov_b32_e32 v23, v36
	v_mov_b32_e32 v24, v32
	v_mov_b32_e32 v25, v34

.LBB0_1045:
	v_add_u32_e32 v18, 0xb0, v6
	v_lshlrev_b32_e32 v6, 5, v18
	v_and_or_b32 v6, v6, s67, v30
	v_lshlrev_b32_e32 v194, 3, v6
	v_pk_mul_f32 v[22:23], v[80:81], s[28:29] op_sel_hi:[1,0]
	v_pk_mul_f32 v[14:15], v[78:79], s[28:29] op_sel_hi:[1,0]
	v_pk_mul_f32 v[20:21], v[76:77], s[28:29] op_sel_hi:[1,0]
	v_pk_mul_f32 v[16:17], v[74:75], s[28:29] op_sel_hi:[1,0]
	s_and_b64 vcc, exec, s[4:5]
	v_lshl_add_u64 v[12:13], s[18:19], 0, v[194:195]
	s_cbranch_vccnz .LBB0_1047
	s_waitcnt vmcnt(2)
	v_mov_b32_e32 v30, v232
	v_mov_b32_e32 v31, v233
	v_mov_b32_e32 v32, v234
	v_mov_b32_e32 v33, v235
	v_mov_b32_e32 v34, v236
	v_mov_b32_e32 v35, v237
	v_mov_b32_e32 v36, v238
	v_mov_b32_e32 v37, v239
	v_mov_b32_e32 v224, v30
	v_mov_b32_e32 v225, v31
	v_mov_b32_e32 v226, v32
	v_mov_b32_e32 v227, v33
	v_mov_b32_e32 v228, v34
	v_mov_b32_e32 v229, v35
	v_mov_b32_e32 v230, v36
	v_mov_b32_e32 v231, v37
	v_pk_mul_f32 v[24:25], v[14:15], v[30:31] op_sel:[1,1] op_sel_hi:[1,0]
	v_mul_f32_e32 v38, v23, v33
	v_mul_f32_e32 v40, v23, v32
	v_pk_mul_f32 v[44:45], v[16:17], v[34:35] op_sel:[1,1] op_sel_hi:[1,0]
	v_mul_f32_e32 v46, v21, v37
	v_mul_f32_e32 v48, v21, v36
	v_pk_mul_f32 v[6:7], v[14:15], v[30:31]
	v_pk_mul_f32 v[42:43], v[16:17], v[34:35]
	v_pk_fma_f32 v[14:15], v[14:15], v[30:31], v[24:25] op_sel_hi:[0,1,1]
	v_pk_fma_f32 v[30:31], v[22:23], v[32:33], v[38:39] op_sel_hi:[1,1,0] neg_lo:[0,0,1] neg_hi:[0,0,1]
	v_pk_fma_f32 v[32:33], v[22:23], v[32:33], v[40:41] op_sel:[0,1,0] op_sel_hi:[1,0,0]
	v_pk_fma_f32 v[16:17], v[16:17], v[34:35], v[44:45] op_sel_hi:[0,1,1]
	v_pk_fma_f32 v[22:23], v[20:21], v[36:37], v[46:47] op_sel_hi:[1,1,0] neg_lo:[0,0,1] neg_hi:[0,0,1]
	v_pk_fma_f32 v[34:35], v[20:21], v[36:37], v[48:49] op_sel:[0,1,0] op_sel_hi:[1,0,0]
	v_sub_f32_e32 v16, v42, v44
	v_sub_f32_e32 v14, v6, v24
	v_mov_b32_e32 v20, v22
	v_mov_b32_e32 v21, v34
	v_mov_b32_e32 v22, v30
	v_mov_b32_e32 v23, v32
